# combo11 + nt on the P10 final-output stores (268 MB written once, never re-read): keeps the gate matrix / expert-v operands in the caches
# speedup vs baseline: 1.0105x; 1.0041x over previous
.LBB0_1361:
	s_andn2_b64 vcc, exec, s[0:1]
	s_mov_b64 s[0:1], -1
	s_ashr_i32 s17, s24, 4
	s_mul_hi_i32 s19, s17, 0x18000
	s_mul_i32 s17, s17, 0x18000
	s_add_u32 s26, s45, s17
	s_addc_u32 s27, s46, s19
	v_lshl_or_b32 v238, s54, 8, v223
	v_mov_b32_e32 v239, 0
	v_lshl_add_u64 v[240:241], v[238:239], 2, s[26:27]
	global_load_dwordx4 v[176:179], v[240:241], off
	global_load_dwordx4 v[180:183], v[240:241], off offset:64
	global_load_dwordx4 v[184:187], v[240:241], off offset:512
	global_load_dwordx4 v[188:191], v[240:241], off offset:576
	v_lshl_add_u32 v242, s24, 8, v206
	v_mov_b32_e32 v243, 0
	v_lshlrev_b64 v[192:193], 13, v[242:243]
	v_lshl_add_u64 v[192:193], v[192:193], 0, s[8:9]
	v_and_b32_e32 v244, 12, v223
	v_add_u32_e32 v244, v244, v238
	v_mov_b32_e32 v245, 0
	v_lshl_add_u64 v[192:193], v[244:245], 1, v[192:193]
	v_and_b32_e32 v242, -9, v206
	v_lshl_add_u32 v242, s24, 8, v242
	v_lshlrev_b64 v[194:195], 14, v[242:243]
	v_lshl_add_u64 v[194:195], v[194:195], 0, s[4:5]
	v_lshl_add_u64 v[194:195], v[238:239], 2, v[194:195]
	v_and_b32_e32 v244, 8, v206
	v_lshlrev_b32_e32 v244, 3, v244
	v_lshl_add_u64 v[194:195], v[244:245], 0, v[194:195]
	s_mov_b32 s26, 0x0
	s_mov_b32 s27, 0
	v_lshl_add_u64 v[196:197], v[192:193], 0, s[26:27]
	global_load_dwordx4 v[0:3], v[196:197], off
	s_mov_b32 s26, 0x0
	s_mov_b32 s27, 0
	v_lshl_add_u64 v[196:197], v[192:193], 0, s[26:27]
	global_load_dwordx4 v[4:7], v[196:197], off offset:256
	s_mov_b32 s26, 0x20000
	s_mov_b32 s27, 0
	v_lshl_add_u64 v[196:197], v[192:193], 0, s[26:27]
	global_load_dwordx4 v[8:11], v[196:197], off
	s_mov_b32 s26, 0x20000
	s_mov_b32 s27, 0
	v_lshl_add_u64 v[196:197], v[192:193], 0, s[26:27]
	global_load_dwordx4 v[12:15], v[196:197], off offset:256
	s_mov_b32 s26, 0x40000
	s_mov_b32 s27, 0
	v_lshl_add_u64 v[196:197], v[192:193], 0, s[26:27]
	global_load_dwordx4 v[16:19], v[196:197], off
	s_mov_b32 s26, 0x40000
	s_mov_b32 s27, 0
	v_lshl_add_u64 v[196:197], v[192:193], 0, s[26:27]
	global_load_dwordx4 v[20:23], v[196:197], off offset:256
	s_mov_b32 s26, 0x60000
	s_mov_b32 s27, 0
	v_lshl_add_u64 v[196:197], v[192:193], 0, s[26:27]
	global_load_dwordx4 v[24:27], v[196:197], off
	s_mov_b32 s26, 0x60000
	s_mov_b32 s27, 0
	v_lshl_add_u64 v[196:197], v[192:193], 0, s[26:27]
	global_load_dwordx4 v[28:31], v[196:197], off offset:256
	s_waitcnt vmcnt(8)
	v_mul_f32_e32 v176, s14, v176
	v_mul_f32_e32 v177, s14, v177
	v_mul_f32_e32 v178, s14, v178
	v_mul_f32_e32 v179, s14, v179
	v_mul_f32_e32 v180, s14, v180
	v_mul_f32_e32 v181, s14, v181
	v_mul_f32_e32 v182, s14, v182
	v_mul_f32_e32 v183, s14, v183
	v_mul_f32_e32 v184, s14, v184
	v_mul_f32_e32 v185, s14, v185
	v_mul_f32_e32 v186, s14, v186
	v_mul_f32_e32 v187, s14, v187
	v_mul_f32_e32 v188, s14, v188
	v_mul_f32_e32 v189, s14, v189
	v_mul_f32_e32 v190, s14, v190
	v_mul_f32_e32 v191, s14, v191
	s_waitcnt vmcnt(7)
	v_permlane16_swap_b32_e32 v0, v2
	v_permlane16_swap_b32_e32 v1, v3
	s_nop 1
	v_permlane32_swap_b32_e32 v0, v2
	v_permlane32_swap_b32_e32 v1, v3
	s_nop 1
	v_lshlrev_b32_e32 v226, 16, v0
	v_and_b32_e32 v227, 0xffff0000, v0
	v_lshlrev_b32_e32 v228, 16, v1
	v_and_b32_e32 v229, 0xffff0000, v1
	v_lshlrev_b32_e32 v230, 16, v2
	v_and_b32_e32 v231, 0xffff0000, v2
	v_lshlrev_b32_e32 v232, 16, v3
	v_and_b32_e32 v233, 0xffff0000, v3
	v_fma_f32 v226, v156, v176, v226
	v_fma_f32 v227, v157, v177, v227
	v_fma_f32 v228, v158, v178, v228
	v_fma_f32 v229, v159, v179, v229
	v_fma_f32 v230, v152, v180, v230
	v_fma_f32 v231, v153, v181, v231
	v_fma_f32 v232, v154, v182, v232
	v_fma_f32 v233, v155, v183, v233
	v_mov_b32_e32 v234, v230
	v_mov_b32_e32 v235, v231
	v_mov_b32_e32 v236, v232
	v_mov_b32_e32 v237, v233
	s_mov_b32 s26, 0x0
	s_mov_b32 s27, 0
	v_lshl_add_u64 v[198:199], v[194:195], 0, s[26:27]
	v_mov_b32_dpp v230, v226 row_ror:8 row_mask:0xf bank_mask:0x3
	v_mov_b32_dpp v231, v227 row_ror:8 row_mask:0xf bank_mask:0x3
	v_mov_b32_dpp v232, v228 row_ror:8 row_mask:0xf bank_mask:0x3
	v_mov_b32_dpp v233, v229 row_ror:8 row_mask:0xf bank_mask:0x3
	v_mov_b32_dpp v226, v234 row_ror:8 row_mask:0xf bank_mask:0xc
	v_mov_b32_dpp v227, v235 row_ror:8 row_mask:0xf bank_mask:0xc
	v_mov_b32_dpp v228, v236 row_ror:8 row_mask:0xf bank_mask:0xc
	v_mov_b32_dpp v229, v237 row_ror:8 row_mask:0xf bank_mask:0xc
	global_store_dwordx4 v[198:199], v[226:229], off nt
	s_mov_b32 s26, 0x20000
	s_mov_b32 s27, 0
	v_lshl_add_u64 v[198:199], v[198:199], 0, s[26:27]
	global_store_dwordx4 v[198:199], v[230:233], off nt
	s_nop 1
	s_mov_b32 s26, 0x100000
	s_mov_b32 s27, 0
	v_lshl_add_u64 v[196:197], v[192:193], 0, s[26:27]
	global_load_dwordx4 v[0:3], v[196:197], off
	s_waitcnt vmcnt(9)
	v_permlane16_swap_b32_e32 v4, v6
	v_permlane16_swap_b32_e32 v5, v7
	s_nop 1
	v_permlane32_swap_b32_e32 v4, v6
	v_permlane32_swap_b32_e32 v5, v7
	s_nop 1
	v_lshlrev_b32_e32 v226, 16, v4
	v_and_b32_e32 v227, 0xffff0000, v4
	v_lshlrev_b32_e32 v228, 16, v5
	v_and_b32_e32 v229, 0xffff0000, v5
	v_lshlrev_b32_e32 v230, 16, v6
	v_and_b32_e32 v231, 0xffff0000, v6
	v_lshlrev_b32_e32 v232, 16, v7
	v_and_b32_e32 v233, 0xffff0000, v7
	v_fma_f32 v226, v148, v184, v226
	v_fma_f32 v227, v149, v185, v227
	v_fma_f32 v228, v150, v186, v228
	v_fma_f32 v229, v151, v187, v229
	v_fma_f32 v230, v140, v188, v230
	v_fma_f32 v231, v141, v189, v231
	v_fma_f32 v232, v142, v190, v232
	v_fma_f32 v233, v143, v191, v233
	v_mov_b32_e32 v234, v230
	v_mov_b32_e32 v235, v231
	v_mov_b32_e32 v236, v232
	v_mov_b32_e32 v237, v233
	s_mov_b32 s26, 0x0
	s_mov_b32 s27, 0
	v_lshl_add_u64 v[198:199], v[194:195], 0, s[26:27]
	v_mov_b32_dpp v230, v226 row_ror:8 row_mask:0xf bank_mask:0x3
	v_mov_b32_dpp v231, v227 row_ror:8 row_mask:0xf bank_mask:0x3
	v_mov_b32_dpp v232, v228 row_ror:8 row_mask:0xf bank_mask:0x3
	v_mov_b32_dpp v233, v229 row_ror:8 row_mask:0xf bank_mask:0x3
	v_mov_b32_dpp v226, v234 row_ror:8 row_mask:0xf bank_mask:0xc
	v_mov_b32_dpp v227, v235 row_ror:8 row_mask:0xf bank_mask:0xc
	v_mov_b32_dpp v228, v236 row_ror:8 row_mask:0xf bank_mask:0xc
	v_mov_b32_dpp v229, v237 row_ror:8 row_mask:0xf bank_mask:0xc
	global_store_dwordx4 v[198:199], v[226:229], off offset:512 nt
	s_mov_b32 s26, 0x20000
	s_mov_b32 s27, 0
	v_lshl_add_u64 v[198:199], v[198:199], 0, s[26:27]
	global_store_dwordx4 v[198:199], v[230:233], off offset:512 nt
	s_nop 1
	s_mov_b32 s26, 0x100000
	s_mov_b32 s27, 0
	v_lshl_add_u64 v[196:197], v[192:193], 0, s[26:27]
	global_load_dwordx4 v[4:7], v[196:197], off offset:256
	s_waitcnt vmcnt(11)
	v_permlane16_swap_b32_e32 v8, v10
	v_permlane16_swap_b32_e32 v9, v11
	s_nop 1
	v_permlane32_swap_b32_e32 v8, v10
	v_permlane32_swap_b32_e32 v9, v11
	s_nop 1
	v_lshlrev_b32_e32 v226, 16, v8
	v_and_b32_e32 v227, 0xffff0000, v8
	v_lshlrev_b32_e32 v228, 16, v9
	v_and_b32_e32 v229, 0xffff0000, v9
	v_lshlrev_b32_e32 v230, 16, v10
	v_and_b32_e32 v231, 0xffff0000, v10
	v_lshlrev_b32_e32 v232, 16, v11
	v_and_b32_e32 v233, 0xffff0000, v11
	v_fma_f32 v226, v144, v176, v226
	v_fma_f32 v227, v145, v177, v227
	v_fma_f32 v228, v146, v178, v228
	v_fma_f32 v229, v147, v179, v229
	v_fma_f32 v230, v136, v180, v230
	v_fma_f32 v231, v137, v181, v231
	v_fma_f32 v232, v138, v182, v232
	v_fma_f32 v233, v139, v183, v233
	v_mov_b32_e32 v234, v230
	v_mov_b32_e32 v235, v231
	v_mov_b32_e32 v236, v232
	v_mov_b32_e32 v237, v233
	s_mov_b32 s26, 0x40000
	s_mov_b32 s27, 0
	v_lshl_add_u64 v[198:199], v[194:195], 0, s[26:27]
	v_mov_b32_dpp v230, v226 row_ror:8 row_mask:0xf bank_mask:0x3
	v_mov_b32_dpp v231, v227 row_ror:8 row_mask:0xf bank_mask:0x3
	v_mov_b32_dpp v232, v228 row_ror:8 row_mask:0xf bank_mask:0x3
	v_mov_b32_dpp v233, v229 row_ror:8 row_mask:0xf bank_mask:0x3
	v_mov_b32_dpp v226, v234 row_ror:8 row_mask:0xf bank_mask:0xc
	v_mov_b32_dpp v227, v235 row_ror:8 row_mask:0xf bank_mask:0xc
	v_mov_b32_dpp v228, v236 row_ror:8 row_mask:0xf bank_mask:0xc
	v_mov_b32_dpp v229, v237 row_ror:8 row_mask:0xf bank_mask:0xc
	global_store_dwordx4 v[198:199], v[226:229], off nt
	s_mov_b32 s26, 0x20000
	s_mov_b32 s27, 0
	v_lshl_add_u64 v[198:199], v[198:199], 0, s[26:27]
	global_store_dwordx4 v[198:199], v[230:233], off nt
	s_nop 1
	s_mov_b32 s26, 0x120000
	s_mov_b32 s27, 0
	v_lshl_add_u64 v[196:197], v[192:193], 0, s[26:27]
	global_load_dwordx4 v[8:11], v[196:197], off
	s_waitcnt vmcnt(13)
	v_permlane16_swap_b32_e32 v12, v14
	v_permlane16_swap_b32_e32 v13, v15
	s_nop 1
	v_permlane32_swap_b32_e32 v12, v14
	v_permlane32_swap_b32_e32 v13, v15
	s_nop 1
	v_lshlrev_b32_e32 v226, 16, v12
	v_and_b32_e32 v227, 0xffff0000, v12
	v_lshlrev_b32_e32 v228, 16, v13
	v_and_b32_e32 v229, 0xffff0000, v13
	v_lshlrev_b32_e32 v230, 16, v14
	v_and_b32_e32 v231, 0xffff0000, v14
	v_lshlrev_b32_e32 v232, 16, v15
	v_and_b32_e32 v233, 0xffff0000, v15
	v_fma_f32 v226, v132, v184, v226
	v_fma_f32 v227, v133, v185, v227
	v_fma_f32 v228, v134, v186, v228
	v_fma_f32 v229, v135, v187, v229
	v_fma_f32 v230, v128, v188, v230
	v_fma_f32 v231, v129, v189, v231
	v_fma_f32 v232, v130, v190, v232
	v_fma_f32 v233, v131, v191, v233
	v_mov_b32_e32 v234, v230
	v_mov_b32_e32 v235, v231
	v_mov_b32_e32 v236, v232
	v_mov_b32_e32 v237, v233
	s_mov_b32 s26, 0x40000
	s_mov_b32 s27, 0
	v_lshl_add_u64 v[198:199], v[194:195], 0, s[26:27]
	v_mov_b32_dpp v230, v226 row_ror:8 row_mask:0xf bank_mask:0x3
	v_mov_b32_dpp v231, v227 row_ror:8 row_mask:0xf bank_mask:0x3
	v_mov_b32_dpp v232, v228 row_ror:8 row_mask:0xf bank_mask:0x3
	v_mov_b32_dpp v233, v229 row_ror:8 row_mask:0xf bank_mask:0x3
	v_mov_b32_dpp v226, v234 row_ror:8 row_mask:0xf bank_mask:0xc
	v_mov_b32_dpp v227, v235 row_ror:8 row_mask:0xf bank_mask:0xc
	v_mov_b32_dpp v228, v236 row_ror:8 row_mask:0xf bank_mask:0xc
	v_mov_b32_dpp v229, v237 row_ror:8 row_mask:0xf bank_mask:0xc
	global_store_dwordx4 v[198:199], v[226:229], off offset:512 nt
	s_mov_b32 s26, 0x20000
	s_mov_b32 s27, 0
	v_lshl_add_u64 v[198:199], v[198:199], 0, s[26:27]
	global_store_dwordx4 v[198:199], v[230:233], off offset:512 nt
	s_nop 1
	s_mov_b32 s26, 0x120000
	s_mov_b32 s27, 0
	v_lshl_add_u64 v[196:197], v[192:193], 0, s[26:27]
	global_load_dwordx4 v[12:15], v[196:197], off offset:256
	s_waitcnt vmcnt(15)
	v_permlane16_swap_b32_e32 v16, v18
	v_permlane16_swap_b32_e32 v17, v19
	s_nop 1
	v_permlane32_swap_b32_e32 v16, v18
	v_permlane32_swap_b32_e32 v17, v19
	s_nop 1
	v_lshlrev_b32_e32 v226, 16, v16
	v_and_b32_e32 v227, 0xffff0000, v16
	v_lshlrev_b32_e32 v228, 16, v17
	v_and_b32_e32 v229, 0xffff0000, v17
	v_lshlrev_b32_e32 v230, 16, v18
	v_and_b32_e32 v231, 0xffff0000, v18
	v_lshlrev_b32_e32 v232, 16, v19
	v_and_b32_e32 v233, 0xffff0000, v19
	v_fma_f32 v226, v124, v176, v226
	v_fma_f32 v227, v125, v177, v227
	v_fma_f32 v228, v126, v178, v228
	v_fma_f32 v229, v127, v179, v229
	v_fma_f32 v230, v120, v180, v230
	v_fma_f32 v231, v121, v181, v231
	v_fma_f32 v232, v122, v182, v232
	v_fma_f32 v233, v123, v183, v233
	v_mov_b32_e32 v234, v230
	v_mov_b32_e32 v235, v231
	v_mov_b32_e32 v236, v232
	v_mov_b32_e32 v237, v233
	s_mov_b32 s26, 0x80000
	s_mov_b32 s27, 0
	v_lshl_add_u64 v[198:199], v[194:195], 0, s[26:27]
	v_mov_b32_dpp v230, v226 row_ror:8 row_mask:0xf bank_mask:0x3
	v_mov_b32_dpp v231, v227 row_ror:8 row_mask:0xf bank_mask:0x3
	v_mov_b32_dpp v232, v228 row_ror:8 row_mask:0xf bank_mask:0x3
	v_mov_b32_dpp v233, v229 row_ror:8 row_mask:0xf bank_mask:0x3
	v_mov_b32_dpp v226, v234 row_ror:8 row_mask:0xf bank_mask:0xc
	v_mov_b32_dpp v227, v235 row_ror:8 row_mask:0xf bank_mask:0xc
	v_mov_b32_dpp v228, v236 row_ror:8 row_mask:0xf bank_mask:0xc
	v_mov_b32_dpp v229, v237 row_ror:8 row_mask:0xf bank_mask:0xc
	global_store_dwordx4 v[198:199], v[226:229], off nt
	s_mov_b32 s26, 0x20000
	s_mov_b32 s27, 0
	v_lshl_add_u64 v[198:199], v[198:199], 0, s[26:27]
	global_store_dwordx4 v[198:199], v[230:233], off nt
	s_nop 1
	s_mov_b32 s26, 0x140000
	s_mov_b32 s27, 0
	v_lshl_add_u64 v[196:197], v[192:193], 0, s[26:27]
	global_load_dwordx4 v[16:19], v[196:197], off
	s_waitcnt vmcnt(17)
	v_permlane16_swap_b32_e32 v20, v22
	v_permlane16_swap_b32_e32 v21, v23
	s_nop 1
	v_permlane32_swap_b32_e32 v20, v22
	v_permlane32_swap_b32_e32 v21, v23
	s_nop 1
	v_lshlrev_b32_e32 v226, 16, v20
	v_and_b32_e32 v227, 0xffff0000, v20
	v_lshlrev_b32_e32 v228, 16, v21
	v_and_b32_e32 v229, 0xffff0000, v21
	v_lshlrev_b32_e32 v230, 16, v22
	v_and_b32_e32 v231, 0xffff0000, v22
	v_lshlrev_b32_e32 v232, 16, v23
	v_and_b32_e32 v233, 0xffff0000, v23
	v_fma_f32 v226, v116, v184, v226
	v_fma_f32 v227, v117, v185, v227
	v_fma_f32 v228, v118, v186, v228
	v_fma_f32 v229, v119, v187, v229
	v_fma_f32 v230, v108, v188, v230
	v_fma_f32 v231, v109, v189, v231
	v_fma_f32 v232, v110, v190, v232
	v_fma_f32 v233, v111, v191, v233
	v_mov_b32_e32 v234, v230
	v_mov_b32_e32 v235, v231
	v_mov_b32_e32 v236, v232
	v_mov_b32_e32 v237, v233
	s_mov_b32 s26, 0x80000
	s_mov_b32 s27, 0
	v_lshl_add_u64 v[198:199], v[194:195], 0, s[26:27]
	v_mov_b32_dpp v230, v226 row_ror:8 row_mask:0xf bank_mask:0x3
	v_mov_b32_dpp v231, v227 row_ror:8 row_mask:0xf bank_mask:0x3
	v_mov_b32_dpp v232, v228 row_ror:8 row_mask:0xf bank_mask:0x3
	v_mov_b32_dpp v233, v229 row_ror:8 row_mask:0xf bank_mask:0x3
	v_mov_b32_dpp v226, v234 row_ror:8 row_mask:0xf bank_mask:0xc
	v_mov_b32_dpp v227, v235 row_ror:8 row_mask:0xf bank_mask:0xc
	v_mov_b32_dpp v228, v236 row_ror:8 row_mask:0xf bank_mask:0xc
	v_mov_b32_dpp v229, v237 row_ror:8 row_mask:0xf bank_mask:0xc
	global_store_dwordx4 v[198:199], v[226:229], off offset:512 nt
	s_mov_b32 s26, 0x20000
	s_mov_b32 s27, 0
	v_lshl_add_u64 v[198:199], v[198:199], 0, s[26:27]
	global_store_dwordx4 v[198:199], v[230:233], off offset:512 nt
	s_nop 1
	s_mov_b32 s26, 0x140000
	s_mov_b32 s27, 0
	v_lshl_add_u64 v[196:197], v[192:193], 0, s[26:27]
	global_load_dwordx4 v[20:23], v[196:197], off offset:256
	s_waitcnt vmcnt(19)
	v_permlane16_swap_b32_e32 v24, v26
	v_permlane16_swap_b32_e32 v25, v27
	s_nop 1
	v_permlane32_swap_b32_e32 v24, v26
	v_permlane32_swap_b32_e32 v25, v27
	s_nop 1
	v_lshlrev_b32_e32 v226, 16, v24
	v_and_b32_e32 v227, 0xffff0000, v24
	v_lshlrev_b32_e32 v228, 16, v25
	v_and_b32_e32 v229, 0xffff0000, v25
	v_lshlrev_b32_e32 v230, 16, v26
	v_and_b32_e32 v231, 0xffff0000, v26
	v_lshlrev_b32_e32 v232, 16, v27
	v_and_b32_e32 v233, 0xffff0000, v27
	v_fma_f32 v226, v112, v176, v226
	v_fma_f32 v227, v113, v177, v227
	v_fma_f32 v228, v114, v178, v228
	v_fma_f32 v229, v115, v179, v229
	v_fma_f32 v230, v104, v180, v230
	v_fma_f32 v231, v105, v181, v231
	v_fma_f32 v232, v106, v182, v232
	v_fma_f32 v233, v107, v183, v233
	v_mov_b32_e32 v234, v230
	v_mov_b32_e32 v235, v231
	v_mov_b32_e32 v236, v232
	v_mov_b32_e32 v237, v233
	s_mov_b32 s26, 0xc0000
	s_mov_b32 s27, 0
	v_lshl_add_u64 v[198:199], v[194:195], 0, s[26:27]
	v_mov_b32_dpp v230, v226 row_ror:8 row_mask:0xf bank_mask:0x3
	v_mov_b32_dpp v231, v227 row_ror:8 row_mask:0xf bank_mask:0x3
	v_mov_b32_dpp v232, v228 row_ror:8 row_mask:0xf bank_mask:0x3
	v_mov_b32_dpp v233, v229 row_ror:8 row_mask:0xf bank_mask:0x3
	v_mov_b32_dpp v226, v234 row_ror:8 row_mask:0xf bank_mask:0xc
	v_mov_b32_dpp v227, v235 row_ror:8 row_mask:0xf bank_mask:0xc
	v_mov_b32_dpp v228, v236 row_ror:8 row_mask:0xf bank_mask:0xc
	v_mov_b32_dpp v229, v237 row_ror:8 row_mask:0xf bank_mask:0xc
	global_store_dwordx4 v[198:199], v[226:229], off nt
	s_mov_b32 s26, 0x20000
	s_mov_b32 s27, 0
	v_lshl_add_u64 v[198:199], v[198:199], 0, s[26:27]
	global_store_dwordx4 v[198:199], v[230:233], off nt
	s_nop 1
	s_mov_b32 s26, 0x160000
	s_mov_b32 s27, 0
	v_lshl_add_u64 v[196:197], v[192:193], 0, s[26:27]
	global_load_dwordx4 v[24:27], v[196:197], off
	s_waitcnt vmcnt(21)
	v_permlane16_swap_b32_e32 v28, v30
	v_permlane16_swap_b32_e32 v29, v31
	s_nop 1
	v_permlane32_swap_b32_e32 v28, v30
	v_permlane32_swap_b32_e32 v29, v31
	s_nop 1
	v_lshlrev_b32_e32 v226, 16, v28
	v_and_b32_e32 v227, 0xffff0000, v28
	v_lshlrev_b32_e32 v228, 16, v29
	v_and_b32_e32 v229, 0xffff0000, v29
	v_lshlrev_b32_e32 v230, 16, v30
	v_and_b32_e32 v231, 0xffff0000, v30
	v_lshlrev_b32_e32 v232, 16, v31
	v_and_b32_e32 v233, 0xffff0000, v31
	v_fma_f32 v226, v100, v184, v226
	v_fma_f32 v227, v101, v185, v227
	v_fma_f32 v228, v102, v186, v228
	v_fma_f32 v229, v103, v187, v229
	v_fma_f32 v230, v96, v188, v230
	v_fma_f32 v231, v97, v189, v231
	v_fma_f32 v232, v98, v190, v232
	v_fma_f32 v233, v99, v191, v233
	v_mov_b32_e32 v234, v230
	v_mov_b32_e32 v235, v231
	v_mov_b32_e32 v236, v232
	v_mov_b32_e32 v237, v233
	s_mov_b32 s26, 0xc0000
	s_mov_b32 s27, 0
	v_lshl_add_u64 v[198:199], v[194:195], 0, s[26:27]
	v_mov_b32_dpp v230, v226 row_ror:8 row_mask:0xf bank_mask:0x3
	v_mov_b32_dpp v231, v227 row_ror:8 row_mask:0xf bank_mask:0x3
	v_mov_b32_dpp v232, v228 row_ror:8 row_mask:0xf bank_mask:0x3
	v_mov_b32_dpp v233, v229 row_ror:8 row_mask:0xf bank_mask:0x3
	v_mov_b32_dpp v226, v234 row_ror:8 row_mask:0xf bank_mask:0xc
	v_mov_b32_dpp v227, v235 row_ror:8 row_mask:0xf bank_mask:0xc
	v_mov_b32_dpp v228, v236 row_ror:8 row_mask:0xf bank_mask:0xc
	v_mov_b32_dpp v229, v237 row_ror:8 row_mask:0xf bank_mask:0xc
	global_store_dwordx4 v[198:199], v[226:229], off offset:512 nt
	s_mov_b32 s26, 0x20000
	s_mov_b32 s27, 0
	v_lshl_add_u64 v[198:199], v[198:199], 0, s[26:27]
	global_store_dwordx4 v[198:199], v[230:233], off offset:512 nt
	s_nop 1
	s_mov_b32 s26, 0x160000
	s_mov_b32 s27, 0
	v_lshl_add_u64 v[196:197], v[192:193], 0, s[26:27]
	global_load_dwordx4 v[28:31], v[196:197], off offset:256
	s_waitcnt vmcnt(21)
	v_permlane16_swap_b32_e32 v0, v2
	v_permlane16_swap_b32_e32 v1, v3
	s_nop 1
	v_permlane32_swap_b32_e32 v0, v2
	v_permlane32_swap_b32_e32 v1, v3
	s_nop 1
	v_lshlrev_b32_e32 v226, 16, v0
	v_and_b32_e32 v227, 0xffff0000, v0
	v_lshlrev_b32_e32 v228, 16, v1
	v_and_b32_e32 v229, 0xffff0000, v1
	v_lshlrev_b32_e32 v230, 16, v2
	v_and_b32_e32 v231, 0xffff0000, v2
	v_lshlrev_b32_e32 v232, 16, v3
	v_and_b32_e32 v233, 0xffff0000, v3
	v_fma_f32 v226, v92, v176, v226
	v_fma_f32 v227, v93, v177, v227
	v_fma_f32 v228, v94, v178, v228
	v_fma_f32 v229, v95, v179, v229
	v_fma_f32 v230, v88, v180, v230
	v_fma_f32 v231, v89, v181, v231
	v_fma_f32 v232, v90, v182, v232
	v_fma_f32 v233, v91, v183, v233
	v_mov_b32_e32 v234, v230
	v_mov_b32_e32 v235, v231
	v_mov_b32_e32 v236, v232
	v_mov_b32_e32 v237, v233
	s_mov_b32 s26, 0x200000
	s_mov_b32 s27, 0
	v_lshl_add_u64 v[198:199], v[194:195], 0, s[26:27]
	v_mov_b32_dpp v230, v226 row_ror:8 row_mask:0xf bank_mask:0x3
	v_mov_b32_dpp v231, v227 row_ror:8 row_mask:0xf bank_mask:0x3
	v_mov_b32_dpp v232, v228 row_ror:8 row_mask:0xf bank_mask:0x3
	v_mov_b32_dpp v233, v229 row_ror:8 row_mask:0xf bank_mask:0x3
	v_mov_b32_dpp v226, v234 row_ror:8 row_mask:0xf bank_mask:0xc
	v_mov_b32_dpp v227, v235 row_ror:8 row_mask:0xf bank_mask:0xc
	v_mov_b32_dpp v228, v236 row_ror:8 row_mask:0xf bank_mask:0xc
	v_mov_b32_dpp v229, v237 row_ror:8 row_mask:0xf bank_mask:0xc
	global_store_dwordx4 v[198:199], v[226:229], off nt
	s_mov_b32 s26, 0x20000
	s_mov_b32 s27, 0
	v_lshl_add_u64 v[198:199], v[198:199], 0, s[26:27]
	global_store_dwordx4 v[198:199], v[230:233], off nt
	s_nop 1
	s_waitcnt vmcnt(20)
	v_permlane16_swap_b32_e32 v4, v6
	v_permlane16_swap_b32_e32 v5, v7
	s_nop 1
	v_permlane32_swap_b32_e32 v4, v6
	v_permlane32_swap_b32_e32 v5, v7
	s_nop 1
	v_lshlrev_b32_e32 v226, 16, v4
	v_and_b32_e32 v227, 0xffff0000, v4
	v_lshlrev_b32_e32 v228, 16, v5
	v_and_b32_e32 v229, 0xffff0000, v5
	v_lshlrev_b32_e32 v230, 16, v6
	v_and_b32_e32 v231, 0xffff0000, v6
	v_lshlrev_b32_e32 v232, 16, v7
	v_and_b32_e32 v233, 0xffff0000, v7
	v_fma_f32 v226, v84, v184, v226
	v_fma_f32 v227, v85, v185, v227
	v_fma_f32 v228, v86, v186, v228
	v_fma_f32 v229, v87, v187, v229
	v_fma_f32 v230, v76, v188, v230
	v_fma_f32 v231, v77, v189, v231
	v_fma_f32 v232, v78, v190, v232
	v_fma_f32 v233, v79, v191, v233
	v_mov_b32_e32 v234, v230
	v_mov_b32_e32 v235, v231
	v_mov_b32_e32 v236, v232
	v_mov_b32_e32 v237, v233
	s_mov_b32 s26, 0x200000
	s_mov_b32 s27, 0
	v_lshl_add_u64 v[198:199], v[194:195], 0, s[26:27]
	v_mov_b32_dpp v230, v226 row_ror:8 row_mask:0xf bank_mask:0x3
	v_mov_b32_dpp v231, v227 row_ror:8 row_mask:0xf bank_mask:0x3
	v_mov_b32_dpp v232, v228 row_ror:8 row_mask:0xf bank_mask:0x3
	v_mov_b32_dpp v233, v229 row_ror:8 row_mask:0xf bank_mask:0x3
	v_mov_b32_dpp v226, v234 row_ror:8 row_mask:0xf bank_mask:0xc
	v_mov_b32_dpp v227, v235 row_ror:8 row_mask:0xf bank_mask:0xc
	v_mov_b32_dpp v228, v236 row_ror:8 row_mask:0xf bank_mask:0xc
	v_mov_b32_dpp v229, v237 row_ror:8 row_mask:0xf bank_mask:0xc
	global_store_dwordx4 v[198:199], v[226:229], off offset:512 nt
	s_mov_b32 s26, 0x20000
	s_mov_b32 s27, 0
	v_lshl_add_u64 v[198:199], v[198:199], 0, s[26:27]
	global_store_dwordx4 v[198:199], v[230:233], off offset:512 nt
	s_nop 1
	s_waitcnt vmcnt(19)
	v_permlane16_swap_b32_e32 v8, v10
	v_permlane16_swap_b32_e32 v9, v11
	s_nop 1
	v_permlane32_swap_b32_e32 v8, v10
	v_permlane32_swap_b32_e32 v9, v11
	s_nop 1
	v_lshlrev_b32_e32 v226, 16, v8
	v_and_b32_e32 v227, 0xffff0000, v8
	v_lshlrev_b32_e32 v228, 16, v9
	v_and_b32_e32 v229, 0xffff0000, v9
	v_lshlrev_b32_e32 v230, 16, v10
	v_and_b32_e32 v231, 0xffff0000, v10
	v_lshlrev_b32_e32 v232, 16, v11
	v_and_b32_e32 v233, 0xffff0000, v11
	v_fma_f32 v226, v80, v176, v226
	v_fma_f32 v227, v81, v177, v227
	v_fma_f32 v228, v82, v178, v228
	v_fma_f32 v229, v83, v179, v229
	v_fma_f32 v230, v72, v180, v230
	v_fma_f32 v231, v73, v181, v231
	v_fma_f32 v232, v74, v182, v232
	v_fma_f32 v233, v75, v183, v233
	v_mov_b32_e32 v234, v230
	v_mov_b32_e32 v235, v231
	v_mov_b32_e32 v236, v232
	v_mov_b32_e32 v237, v233
	s_mov_b32 s26, 0x240000
	s_mov_b32 s27, 0
	v_lshl_add_u64 v[198:199], v[194:195], 0, s[26:27]
	v_mov_b32_dpp v230, v226 row_ror:8 row_mask:0xf bank_mask:0x3
	v_mov_b32_dpp v231, v227 row_ror:8 row_mask:0xf bank_mask:0x3
	v_mov_b32_dpp v232, v228 row_ror:8 row_mask:0xf bank_mask:0x3
	v_mov_b32_dpp v233, v229 row_ror:8 row_mask:0xf bank_mask:0x3
	v_mov_b32_dpp v226, v234 row_ror:8 row_mask:0xf bank_mask:0xc
	v_mov_b32_dpp v227, v235 row_ror:8 row_mask:0xf bank_mask:0xc
	v_mov_b32_dpp v228, v236 row_ror:8 row_mask:0xf bank_mask:0xc
	v_mov_b32_dpp v229, v237 row_ror:8 row_mask:0xf bank_mask:0xc
	global_store_dwordx4 v[198:199], v[226:229], off nt
	s_mov_b32 s26, 0x20000
	s_mov_b32 s27, 0
	v_lshl_add_u64 v[198:199], v[198:199], 0, s[26:27]
	global_store_dwordx4 v[198:199], v[230:233], off nt
	s_nop 1
	s_waitcnt vmcnt(18)
	v_permlane16_swap_b32_e32 v12, v14
	v_permlane16_swap_b32_e32 v13, v15
	s_nop 1
	v_permlane32_swap_b32_e32 v12, v14
	v_permlane32_swap_b32_e32 v13, v15
	s_nop 1
	v_lshlrev_b32_e32 v226, 16, v12
	v_and_b32_e32 v227, 0xffff0000, v12
	v_lshlrev_b32_e32 v228, 16, v13
	v_and_b32_e32 v229, 0xffff0000, v13
	v_lshlrev_b32_e32 v230, 16, v14
	v_and_b32_e32 v231, 0xffff0000, v14
	v_lshlrev_b32_e32 v232, 16, v15
	v_and_b32_e32 v233, 0xffff0000, v15
	v_fma_f32 v226, v68, v184, v226
	v_fma_f32 v227, v69, v185, v227
	v_fma_f32 v228, v70, v186, v228
	v_fma_f32 v229, v71, v187, v229
	v_fma_f32 v230, v60, v188, v230
	v_fma_f32 v231, v61, v189, v231
	v_fma_f32 v232, v62, v190, v232
	v_fma_f32 v233, v63, v191, v233
	v_mov_b32_e32 v234, v230
	v_mov_b32_e32 v235, v231
	v_mov_b32_e32 v236, v232
	v_mov_b32_e32 v237, v233
	s_mov_b32 s26, 0x240000
	s_mov_b32 s27, 0
	v_lshl_add_u64 v[198:199], v[194:195], 0, s[26:27]
	v_mov_b32_dpp v230, v226 row_ror:8 row_mask:0xf bank_mask:0x3
	v_mov_b32_dpp v231, v227 row_ror:8 row_mask:0xf bank_mask:0x3
	v_mov_b32_dpp v232, v228 row_ror:8 row_mask:0xf bank_mask:0x3
	v_mov_b32_dpp v233, v229 row_ror:8 row_mask:0xf bank_mask:0x3
	v_mov_b32_dpp v226, v234 row_ror:8 row_mask:0xf bank_mask:0xc
	v_mov_b32_dpp v227, v235 row_ror:8 row_mask:0xf bank_mask:0xc
	v_mov_b32_dpp v228, v236 row_ror:8 row_mask:0xf bank_mask:0xc
	v_mov_b32_dpp v229, v237 row_ror:8 row_mask:0xf bank_mask:0xc
	global_store_dwordx4 v[198:199], v[226:229], off offset:512 nt
	s_mov_b32 s26, 0x20000
	s_mov_b32 s27, 0
	v_lshl_add_u64 v[198:199], v[198:199], 0, s[26:27]
	global_store_dwordx4 v[198:199], v[230:233], off offset:512 nt
	s_nop 1
	s_waitcnt vmcnt(17)
	v_permlane16_swap_b32_e32 v16, v18
	v_permlane16_swap_b32_e32 v17, v19
	s_nop 1
	v_permlane32_swap_b32_e32 v16, v18
	v_permlane32_swap_b32_e32 v17, v19
	s_nop 1
	v_lshlrev_b32_e32 v226, 16, v16
	v_and_b32_e32 v227, 0xffff0000, v16
	v_lshlrev_b32_e32 v228, 16, v17
	v_and_b32_e32 v229, 0xffff0000, v17
	v_lshlrev_b32_e32 v230, 16, v18
	v_and_b32_e32 v231, 0xffff0000, v18
	v_lshlrev_b32_e32 v232, 16, v19
	v_and_b32_e32 v233, 0xffff0000, v19
	v_fma_f32 v226, v64, v176, v226
	v_fma_f32 v227, v65, v177, v227
	v_fma_f32 v228, v66, v178, v228
	v_fma_f32 v229, v67, v179, v229
	v_fma_f32 v230, v56, v180, v230
	v_fma_f32 v231, v57, v181, v231
	v_fma_f32 v232, v58, v182, v232
	v_fma_f32 v233, v59, v183, v233
	v_mov_b32_e32 v234, v230
	v_mov_b32_e32 v235, v231
	v_mov_b32_e32 v236, v232
	v_mov_b32_e32 v237, v233
	s_mov_b32 s26, 0x280000
	s_mov_b32 s27, 0
	v_lshl_add_u64 v[198:199], v[194:195], 0, s[26:27]
	v_mov_b32_dpp v230, v226 row_ror:8 row_mask:0xf bank_mask:0x3
	v_mov_b32_dpp v231, v227 row_ror:8 row_mask:0xf bank_mask:0x3
	v_mov_b32_dpp v232, v228 row_ror:8 row_mask:0xf bank_mask:0x3
	v_mov_b32_dpp v233, v229 row_ror:8 row_mask:0xf bank_mask:0x3
	v_mov_b32_dpp v226, v234 row_ror:8 row_mask:0xf bank_mask:0xc
	v_mov_b32_dpp v227, v235 row_ror:8 row_mask:0xf bank_mask:0xc
	v_mov_b32_dpp v228, v236 row_ror:8 row_mask:0xf bank_mask:0xc
	v_mov_b32_dpp v229, v237 row_ror:8 row_mask:0xf bank_mask:0xc
	global_store_dwordx4 v[198:199], v[226:229], off nt
	s_mov_b32 s26, 0x20000
	s_mov_b32 s27, 0
	v_lshl_add_u64 v[198:199], v[198:199], 0, s[26:27]
	global_store_dwordx4 v[198:199], v[230:233], off nt
	s_nop 1
	s_waitcnt vmcnt(16)
	v_permlane16_swap_b32_e32 v20, v22
	v_permlane16_swap_b32_e32 v21, v23
	s_nop 1
	v_permlane32_swap_b32_e32 v20, v22
	v_permlane32_swap_b32_e32 v21, v23
	s_nop 1
	v_lshlrev_b32_e32 v226, 16, v20
	v_and_b32_e32 v227, 0xffff0000, v20
	v_lshlrev_b32_e32 v228, 16, v21
	v_and_b32_e32 v229, 0xffff0000, v21
	v_lshlrev_b32_e32 v230, 16, v22
	v_and_b32_e32 v231, 0xffff0000, v22
	v_lshlrev_b32_e32 v232, 16, v23
	v_and_b32_e32 v233, 0xffff0000, v23
	v_fma_f32 v226, v52, v184, v226
	v_fma_f32 v227, v53, v185, v227
	v_fma_f32 v228, v54, v186, v228
	v_fma_f32 v229, v55, v187, v229
	v_fma_f32 v230, v44, v188, v230
	v_fma_f32 v231, v45, v189, v231
	v_fma_f32 v232, v46, v190, v232
	v_fma_f32 v233, v47, v191, v233
	v_mov_b32_e32 v234, v230
	v_mov_b32_e32 v235, v231
	v_mov_b32_e32 v236, v232
	v_mov_b32_e32 v237, v233
	s_mov_b32 s26, 0x280000
	s_mov_b32 s27, 0
	v_lshl_add_u64 v[198:199], v[194:195], 0, s[26:27]
	v_mov_b32_dpp v230, v226 row_ror:8 row_mask:0xf bank_mask:0x3
	v_mov_b32_dpp v231, v227 row_ror:8 row_mask:0xf bank_mask:0x3
	v_mov_b32_dpp v232, v228 row_ror:8 row_mask:0xf bank_mask:0x3
	v_mov_b32_dpp v233, v229 row_ror:8 row_mask:0xf bank_mask:0x3
	v_mov_b32_dpp v226, v234 row_ror:8 row_mask:0xf bank_mask:0xc
	v_mov_b32_dpp v227, v235 row_ror:8 row_mask:0xf bank_mask:0xc
	v_mov_b32_dpp v228, v236 row_ror:8 row_mask:0xf bank_mask:0xc
	v_mov_b32_dpp v229, v237 row_ror:8 row_mask:0xf bank_mask:0xc
	global_store_dwordx4 v[198:199], v[226:229], off offset:512 nt
	s_mov_b32 s26, 0x20000
	s_mov_b32 s27, 0
	v_lshl_add_u64 v[198:199], v[198:199], 0, s[26:27]
	global_store_dwordx4 v[198:199], v[230:233], off offset:512 nt
	s_nop 1
	s_waitcnt vmcnt(15)
	v_permlane16_swap_b32_e32 v24, v26
	v_permlane16_swap_b32_e32 v25, v27
	s_nop 1
	v_permlane32_swap_b32_e32 v24, v26
	v_permlane32_swap_b32_e32 v25, v27
	s_nop 1
	v_lshlrev_b32_e32 v226, 16, v24
	v_and_b32_e32 v227, 0xffff0000, v24
	v_lshlrev_b32_e32 v228, 16, v25
	v_and_b32_e32 v229, 0xffff0000, v25
	v_lshlrev_b32_e32 v230, 16, v26
	v_and_b32_e32 v231, 0xffff0000, v26
	v_lshlrev_b32_e32 v232, 16, v27
	v_and_b32_e32 v233, 0xffff0000, v27
	v_fma_f32 v226, v48, v176, v226
	v_fma_f32 v227, v49, v177, v227
	v_fma_f32 v228, v50, v178, v228
	v_fma_f32 v229, v51, v179, v229
	v_fma_f32 v230, v40, v180, v230
	v_fma_f32 v231, v41, v181, v231
	v_fma_f32 v232, v42, v182, v232
	v_fma_f32 v233, v43, v183, v233
	v_mov_b32_e32 v234, v230
	v_mov_b32_e32 v235, v231
	v_mov_b32_e32 v236, v232
	v_mov_b32_e32 v237, v233
	s_mov_b32 s26, 0x2c0000
	s_mov_b32 s27, 0
	v_lshl_add_u64 v[198:199], v[194:195], 0, s[26:27]
	v_mov_b32_dpp v230, v226 row_ror:8 row_mask:0xf bank_mask:0x3
	v_mov_b32_dpp v231, v227 row_ror:8 row_mask:0xf bank_mask:0x3
	v_mov_b32_dpp v232, v228 row_ror:8 row_mask:0xf bank_mask:0x3
	v_mov_b32_dpp v233, v229 row_ror:8 row_mask:0xf bank_mask:0x3
	v_mov_b32_dpp v226, v234 row_ror:8 row_mask:0xf bank_mask:0xc
	v_mov_b32_dpp v227, v235 row_ror:8 row_mask:0xf bank_mask:0xc
	v_mov_b32_dpp v228, v236 row_ror:8 row_mask:0xf bank_mask:0xc
	v_mov_b32_dpp v229, v237 row_ror:8 row_mask:0xf bank_mask:0xc
	global_store_dwordx4 v[198:199], v[226:229], off nt
	s_mov_b32 s26, 0x20000
	s_mov_b32 s27, 0
	v_lshl_add_u64 v[198:199], v[198:199], 0, s[26:27]
	global_store_dwordx4 v[198:199], v[230:233], off nt
	s_nop 1
	s_waitcnt vmcnt(14)
	v_permlane16_swap_b32_e32 v28, v30
	v_permlane16_swap_b32_e32 v29, v31
	s_nop 1
	v_permlane32_swap_b32_e32 v28, v30
	v_permlane32_swap_b32_e32 v29, v31
	s_nop 1
	v_lshlrev_b32_e32 v226, 16, v28
	v_and_b32_e32 v227, 0xffff0000, v28
	v_lshlrev_b32_e32 v228, 16, v29
	v_and_b32_e32 v229, 0xffff0000, v29
	v_lshlrev_b32_e32 v230, 16, v30
	v_and_b32_e32 v231, 0xffff0000, v30
	v_lshlrev_b32_e32 v232, 16, v31
	v_and_b32_e32 v233, 0xffff0000, v31
	v_fma_f32 v226, v36, v184, v226
	v_fma_f32 v227, v37, v185, v227
	v_fma_f32 v228, v38, v186, v228
	v_fma_f32 v229, v39, v187, v229
	v_fma_f32 v230, v32, v188, v230
	v_fma_f32 v231, v33, v189, v231
	v_fma_f32 v232, v34, v190, v232
	v_fma_f32 v233, v35, v191, v233
	v_mov_b32_e32 v234, v230
	v_mov_b32_e32 v235, v231
	v_mov_b32_e32 v236, v232
	v_mov_b32_e32 v237, v233
	s_mov_b32 s26, 0x2c0000
	s_mov_b32 s27, 0
	v_lshl_add_u64 v[198:199], v[194:195], 0, s[26:27]
	v_mov_b32_dpp v230, v226 row_ror:8 row_mask:0xf bank_mask:0x3
	v_mov_b32_dpp v231, v227 row_ror:8 row_mask:0xf bank_mask:0x3
	v_mov_b32_dpp v232, v228 row_ror:8 row_mask:0xf bank_mask:0x3
	v_mov_b32_dpp v233, v229 row_ror:8 row_mask:0xf bank_mask:0x3
	v_mov_b32_dpp v226, v234 row_ror:8 row_mask:0xf bank_mask:0xc
	v_mov_b32_dpp v227, v235 row_ror:8 row_mask:0xf bank_mask:0xc
	v_mov_b32_dpp v228, v236 row_ror:8 row_mask:0xf bank_mask:0xc
	v_mov_b32_dpp v229, v237 row_ror:8 row_mask:0xf bank_mask:0xc
	global_store_dwordx4 v[198:199], v[226:229], off offset:512 nt
	s_mov_b32 s26, 0x20000
	s_mov_b32 s27, 0
	v_lshl_add_u64 v[198:199], v[198:199], 0, s[26:27]
	global_store_dwordx4 v[198:199], v[230:233], off offset:512 nt
	s_nop 1
	s_cbranch_vccnz .LBB0_1350
	s_andn2_b64 vcc, exec, s[6:7]
	s_cbranch_vccnz .LBB0_1349
	s_barrier
	s_branch .LBB0_1349
